# expert-weight conversion: the f32 expert weights are read exactly once per layer, so their 16 loads carry the nt (streaming) hint to keep the bf16 copies and activations resident in cache; plus previo
# speedup vs baseline: 1.0060x; 1.0043x over previous
; #define LAS __attribute__((address_space(3)))
; #define CE_LOAD(s) do { const float* _b; int _k0, _n0; CE_SRC(s, _b, _k0, _n0); \
;         _Pragma("unroll") for (int _q = 0; _q < 8; ++_q) { const int _i = F.tid + _q * NTHR; v[_q] = *(const f32x4*)(_b + (size_t)(_k0 + (_i >> 6)) * DM + _n0 + (_i & 63) * 4); } } while (0)
; __device__ __forceinline__ void cvt_experts(const Frame& F, const Params& P, int l) {
;     ...
;     int s = F.wg, par = 0;
;     if (s < NS) CE_LOAD(s);
;     for (; s < NS; s += F.nwg, par ^= 1) {
;         LAS float* tl = tile + par * (64 * TP);
; #pragma unroll
;         for (int q = 0; q < 8; ++q) { const int i = F.tid + q * NTHR, r = i >> 6, c = (i & 63) * 4; tl[r * TP + c] = v[q][0]; tl[r * TP + c + 1] = v[q][1]; tl[r * TP + c + 2] = v[q][2]; tl[r * TP + c + 3] = v[q][3]; }
.LBB0_1613:
	s_or_b64 exec, exec, s[8:9]
	v_readlane_b32 s0, v253, 31
	v_readlane_b32 s1, v253, 32
	v_mov_b32_e32 v1, v0
	s_andn2_b64 vcc, exec, s[0:1]
	s_cbranch_vccnz .LBB0_1620
	v_readlane_b32 s0, v253, 34
	s_add_u32 s0, s92, s0
	s_addc_u32 s1, s93, 0
	s_load_dwordx2 s[0:1], s[0:1], 0x0
	v_readlane_b32 s2, v253, 43
	s_add_u32 s8, s87, s2
	v_readlane_b32 s2, v253, 44
	s_addc_u32 s9, 0, s2
	s_lshl_b64 s[8:9], s[8:9], 22
	s_waitcnt lgkmcnt(0)
	s_add_u32 s0, s0, s8
	v_lshlrev_b32_e32 v2, 2, v1
	s_addc_u32 s1, s1, s9
	v_readlane_b32 s2, v254, 1
	s_add_u32 s0, s0, s2
	v_and_b32_e32 v34, 0xfc, v2
	s_addc_u32 s1, s1, 0
	v_lshlrev_b32_e32 v146, 2, v34
	v_add_u32_e32 v54, 0x200, v1
	v_add_u32_e32 v56, 0x400, v1
	v_add_u32_e32 v58, 0x600, v1
	v_add_u32_e32 v18, 0x800, v1
	v_add_u32_e32 v20, 0xa00, v1
	v_add_u32_e32 v28, 0xc00, v1
	v_add_u32_e32 v30, 0xe00, v1
	v_lshl_add_u64 v[26:27], s[0:1], 0, v[146:147]
	v_ashrrev_i32_e32 v35, 6, v1
	v_readlane_b32 s0, v253, 33
	v_ashrrev_i32_e32 v36, 6, v54
	v_ashrrev_i32_e32 v37, 6, v56
	v_ashrrev_i32_e32 v38, 6, v58
	v_ashrrev_i32_e32 v39, 6, v18
	v_ashrrev_i32_e32 v40, 6, v20
	v_ashrrev_i32_e32 v41, 6, v28
	v_ashrrev_i32_e32 v42, 6, v30
	v_add_u32_e32 v2, s0, v35
	v_add_u32_e32 v4, s0, v36
	v_add_u32_e32 v10, s0, v37
	v_add_u32_e32 v12, s0, v38
	v_add_u32_e32 v18, s0, v39
	v_add_u32_e32 v20, s0, v40
	v_add_u32_e32 v28, s0, v41
	v_add_u32_e32 v30, s0, v42
	v_ashrrev_i32_e32 v3, 31, v2
	v_ashrrev_i32_e32 v5, 31, v4
	v_ashrrev_i32_e32 v11, 31, v10
	v_ashrrev_i32_e32 v13, 31, v12
	v_ashrrev_i32_e32 v19, 31, v18
	v_ashrrev_i32_e32 v21, 31, v20
	v_ashrrev_i32_e32 v29, 31, v28
	v_ashrrev_i32_e32 v31, 31, v30
	v_lshlrev_b64 v[2:3], 12, v[2:3]
	v_lshlrev_b64 v[4:5], 12, v[4:5]
	v_lshlrev_b64 v[10:11], 12, v[10:11]
	v_lshlrev_b64 v[12:13], 12, v[12:13]
	v_lshlrev_b64 v[18:19], 12, v[18:19]
	v_lshlrev_b64 v[20:21], 12, v[20:21]
	v_lshlrev_b64 v[28:29], 12, v[28:29]
	v_lshlrev_b64 v[30:31], 12, v[30:31]
	v_lshl_add_u64 v[2:3], v[26:27], 0, v[2:3]
	v_lshl_add_u64 v[6:7], v[26:27], 0, v[4:5]
	v_lshl_add_u64 v[10:11], v[26:27], 0, v[10:11]
	v_lshl_add_u64 v[14:15], v[26:27], 0, v[12:13]
	v_lshl_add_u64 v[18:19], v[26:27], 0, v[18:19]
	v_lshl_add_u64 v[22:23], v[26:27], 0, v[20:21]
	v_lshl_add_u64 v[28:29], v[26:27], 0, v[28:29]
	v_lshl_add_u64 v[30:31], v[26:27], 0, v[30:31]
	global_load_dwordx4 v[2:5], v[2:3], off nt
	s_nop 0
	global_load_dwordx4 v[6:9], v[6:7], off nt
	s_nop 0
	global_load_dwordx4 v[10:13], v[10:11], off nt
	s_nop 0
	global_load_dwordx4 v[14:17], v[14:15], off nt
	s_nop 0
	global_load_dwordx4 v[18:21], v[18:19], off nt
	s_nop 0
	global_load_dwordx4 v[22:25], v[22:23], off nt
	s_nop 0
	global_load_dwordx4 v[26:29], v[28:29], off nt
	s_nop 0
	global_load_dwordx4 v[30:33], v[30:31], off nt
	v_lshlrev_b32_e32 v52, 3, v1
	s_movk_i32 s0, 0x404
	v_ashrrev_i32_e32 v51, 3, v1
	v_and_b32_e32 v60, 56, v52
	v_ashrrev_i32_e32 v54, 3, v54
	v_ashrrev_i32_e32 v56, 3, v56
	v_ashrrev_i32_e32 v58, 3, v58
	v_readlane_b32 s8, v254, 62
	v_mul_lo_u32 v43, v35, s0
	v_mul_lo_u32 v44, v36, s0
	v_mul_lo_u32 v45, v37, s0
	v_mul_lo_u32 v46, v38, s0
	v_mul_lo_u32 v47, v39, s0
	v_mul_lo_u32 v48, v40, s0
	v_mul_lo_u32 v49, v41, s0
	v_mul_lo_u32 v50, v42, s0
	v_mul_u32_u24_e32 v52, 0x404, v60
	v_and_b32_e32 v53, 3, v51
	v_and_b32_e32 v55, 3, v54
	v_and_b32_e32 v57, 3, v56
	v_and_b32_e32 v59, 3, v58
	s_lshl_b32 s0, s96, 8
	s_mov_b32 s1, 0
	v_lshlrev_b32_e32 v146, 1, v60
	v_readlane_b32 s24, v254, 8
	v_readlane_b32 s25, v254, 6
	s_mov_b32 s28, s8
	v_readlane_b32 s9, v254, 63
	s_branch .LBB0_1616

; #define LAS __attribute__((address_space(3)))
; #define CE_LOAD(s) do { const float* _b; int _k0, _n0; CE_SRC(s, _b, _k0, _n0); \
;         _Pragma("unroll") for (int _q = 0; _q < 8; ++_q) { const int _i = F.tid + _q * NTHR; v[_q] = *(const f32x4*)(_b + (size_t)(_k0 + (_i >> 6)) * DM + _n0 + (_i & 63) * 4); } } while (0)
; __device__ __forceinline__ void cvt_experts(const Frame& F, const Params& P, int l) {
;     ...
;     int s = F.wg, par = 0;
;     if (s < NS) CE_LOAD(s);
;     for (; s < NS; s += F.nwg, par ^= 1) {
;         LAS float* tl = tile + par * (64 * TP);
; #pragma unroll
;         for (int q = 0; q < 8; ++q) { const int i = F.tid + q * NTHR, r = i >> 6, c = (i & 63) * 4; tl[r * TP + c] = v[q][0]; tl[r * TP + c + 1] = v[q][1]; tl[r * TP + c + 2] = v[q][2]; tl[r * TP + c + 3] = v[q][3]; }
;         __syncthreads();
;         if (s + F.nwg < NS) CE_LOAD(s + F.nwg);
.LBB0_1618:
	s_andn2_b64 vcc, exec, s[18:19]
	s_cbranch_vccnz .LBB0_1615
	s_mul_hi_i32 s7, s2, 0x2aaaaaab
	s_lshr_b32 s18, s7, 31
	s_ashr_i32 s7, s7, 5
	s_add_i32 s29, s7, s18
	s_mul_i32 s7, s29, 0xffffff40
	s_add_i32 s18, s2, s7
	v_readlane_b32 s7, v254, 7
	s_add_i32 s7, s7, s25
	s_add_i32 s22, s0, s24
	s_and_b32 s40, s7, 0x3c0
	s_and_b32 s41, s22, 0x300
	s_and_b32 s19, s18, 0xffffffc0
	s_cmp_eq_u32 s19, 64
	s_movk_i32 s19, 0xb0
	s_cselect_b32 s19, s19, 0xc0
	s_cmp_gt_u32 s18, 63
	s_cselect_b32 s18, s19, 0xa0
	s_add_u32 s18, s92, s18
	s_addc_u32 s19, s93, 0
	s_load_dwordx2 s[18:19], s[18:19], 0x0
	s_ashr_i32 s31, s29, 31
	s_add_u32 s30, s29, s87
	s_addc_u32 s31, s31, 0
	s_lshl_b64 s[30:31], s[30:31], 22
	s_waitcnt lgkmcnt(0)
	s_add_u32 s18, s18, s30
	s_addc_u32 s19, s19, s31
	s_lshl_b32 s29, s41, 2
	s_add_u32 s18, s18, s29
	s_addc_u32 s19, s19, 0
	v_lshlrev_b32_e32 v2, 2, v34
	v_mov_b32_e32 v3, v147
	v_lshl_add_u64 v[26:27], s[18:19], 0, v[2:3]
	v_add_u32_e32 v2, s40, v35
	v_add_u32_e32 v4, s40, v36
	v_add_u32_e32 v10, s40, v37
	v_add_u32_e32 v12, s40, v38
	v_add_u32_e32 v18, s40, v39
	v_add_u32_e32 v20, s40, v40
	v_add_u32_e32 v28, s40, v41
	v_add_u32_e32 v30, s40, v42
	v_ashrrev_i32_e32 v3, 31, v2
	v_ashrrev_i32_e32 v5, 31, v4
	v_ashrrev_i32_e32 v11, 31, v10
	v_ashrrev_i32_e32 v13, 31, v12
	v_ashrrev_i32_e32 v19, 31, v18
	v_ashrrev_i32_e32 v21, 31, v20
	v_ashrrev_i32_e32 v29, 31, v28
	v_ashrrev_i32_e32 v31, 31, v30
	v_lshlrev_b64 v[2:3], 12, v[2:3]
	v_lshlrev_b64 v[4:5], 12, v[4:5]
	v_lshlrev_b64 v[10:11], 12, v[10:11]
	v_lshlrev_b64 v[12:13], 12, v[12:13]
	v_lshlrev_b64 v[18:19], 12, v[18:19]
	v_lshlrev_b64 v[20:21], 12, v[20:21]
	v_lshlrev_b64 v[28:29], 12, v[28:29]
	v_lshlrev_b64 v[30:31], 12, v[30:31]
	v_lshl_add_u64 v[2:3], v[26:27], 0, v[2:3]
	v_lshl_add_u64 v[6:7], v[26:27], 0, v[4:5]
	v_lshl_add_u64 v[10:11], v[26:27], 0, v[10:11]
	v_lshl_add_u64 v[14:15], v[26:27], 0, v[12:13]
	v_lshl_add_u64 v[18:19], v[26:27], 0, v[18:19]
	v_lshl_add_u64 v[22:23], v[26:27], 0, v[20:21]
	v_lshl_add_u64 v[28:29], v[26:27], 0, v[28:29]
	v_lshl_add_u64 v[30:31], v[26:27], 0, v[30:31]
	global_load_dwordx4 v[2:5], v[2:3], off nt
	s_nop 0
	global_load_dwordx4 v[6:9], v[6:7], off nt
	s_nop 0
	global_load_dwordx4 v[10:13], v[10:11], off nt
	s_nop 0
	global_load_dwordx4 v[14:17], v[14:15], off nt
	s_nop 0
	global_load_dwordx4 v[18:21], v[18:19], off nt
	s_nop 0
	global_load_dwordx4 v[22:25], v[22:23], off nt
	s_nop 0
	global_load_dwordx4 v[26:29], v[28:29], off nt
	s_nop 0
	global_load_dwordx4 v[30:33], v[30:31], off nt
	s_branch .LBB0_1615
